# speedup vs baseline: 1.1206x; 1.0124x over previous
.Lrec_tail:
	s_add_i32 s14, s46, 1
	s_lshl_b32 s6, s14, 13
	s_lshl_b32 s7, s14, 17
	s_and_b32 s6, s6, 0x8000
	s_and_b32 s7, s7, 0x60000
	v_add_u32_e32 v242, s7, v27
	v_add_u32_e32 v243, s7, v28
	v_add_u32_e32 v244, s7, v29
	v_add_u32_e32 v245, s7, v30
	v_permlane32_swap_b32_e32 v10, v46
	v_permlane32_swap_b32_e32 v14, v50
	v_permlane32_swap_b32_e32 v18, v2
	v_permlane32_swap_b32_e32 v22, v250
	v_add_f32_e32 v10, v10, v46
	v_add_f32_e32 v14, v14, v50
	v_add_f32_e32 v18, v18, v2
	v_add_f32_e32 v22, v22, v250
	ds_write2_b32 v31, v10, v14 offset0:0 offset1:16
	ds_write2_b32 v35, v18, v22 offset0:0 offset1:16
	v_permlane32_swap_b32_e32 v11, v47
	v_permlane32_swap_b32_e32 v15, v51
	v_permlane32_swap_b32_e32 v19, v3
	v_permlane32_swap_b32_e32 v23, v251
	v_add_f32_e32 v11, v11, v47
	v_add_f32_e32 v15, v15, v51
	v_add_f32_e32 v19, v19, v3
	v_add_f32_e32 v23, v23, v251
	ds_write2_b32 v32, v11, v15 offset0:0 offset1:16
	ds_write2_b32 v36, v19, v23 offset0:0 offset1:16
	v_permlane32_swap_b32_e32 v12, v48
	v_permlane32_swap_b32_e32 v16, v52
	v_permlane32_swap_b32_e32 v20, v4
	v_permlane32_swap_b32_e32 v24, v252
	v_add_f32_e32 v12, v12, v48
	v_add_f32_e32 v16, v16, v52
	v_add_f32_e32 v20, v20, v4
	v_add_f32_e32 v24, v24, v252
	ds_write2_b32 v33, v12, v16 offset0:0 offset1:16
	ds_write2_b32 v37, v20, v24 offset0:0 offset1:16
	v_permlane32_swap_b32_e32 v13, v49
	v_permlane32_swap_b32_e32 v17, v53
	v_permlane32_swap_b32_e32 v21, v5
	v_permlane32_swap_b32_e32 v25, v253
	v_add_f32_e32 v13, v13, v49
	v_add_f32_e32 v17, v17, v53
	v_add_f32_e32 v21, v21, v5
	v_add_f32_e32 v25, v25, v253
	ds_write2_b32 v34, v13, v17 offset0:0 offset1:16
	ds_write2_b32 v38, v21, v25 offset0:0 offset1:16
	s_waitcnt lgkmcnt(0)
	s_barrier
	ds_read_b128 v[10:13], v9
	ds_read_b128 v[14:17], v9 offset:4096
	ds_read_b128 v[18:21], v9 offset:8192
	ds_read_b128 v[22:25], v9 offset:12288
	s_min_u32 s29, s46, 0xfd
	s_lshl_b32 s29, s29, 19
	s_add_u32 s29, s29, s36
	v_mov_b32_e32 v54, s29
	v_add_co_u32_e32 v54, vcc, v254, v54
	s_nop 1
	v_addc_co_u32_e32 v55, vcc, 0, v255, vcc
	global_load_dwordx2 v[40:41], v[54:55], off
	s_waitcnt lgkmcnt(2)
	v_pk_add_f32 v[10:11], v[10:11], v[14:15]
	v_pk_add_f32 v[12:13], v[12:13], v[16:17]
	s_waitcnt lgkmcnt(0)
	v_pk_add_f32 v[18:19], v[18:19], v[22:23]
	v_pk_add_f32 v[20:21], v[20:21], v[24:25]
	v_pk_add_f32 v[10:11], v[10:11], v[18:19]
	v_pk_add_f32 v[12:13], v[12:13], v[20:21]
	v_fmac_f32_e32 v247, s48, v11
	v_fmac_f32_e32 v246, s48, v10
	v_fmac_f32_e32 v249, s48, v13
	v_fmac_f32_e32 v248, s47, v12
	v_exp_f32_e32 v15, v247
	v_exp_f32_e32 v14, v246
	v_exp_f32_e32 v17, v249
	v_max_f32_e32 v16, 0, v248
	v_add_f32_e32 v15, 1.0, v15
	v_add_f32_e32 v14, 1.0, v14
	v_add_f32_e32 v17, 1.0, v17
	v_rcp_f32_e32 v14, v14
	v_rcp_f32_e32 v15, v15
	v_rcp_f32_e32 v17, v17
	v_add_u32_e32 v18, s7, v1
	v_mul_f32_e32 v12, v16, v14
	v_fmac_f32_e32 v12, v44, v15
	v_max_f32_e32 v19, 0, v12
	v_mul_f32_e32 v13, v17, v19
	v_fma_mixlo_f16 v14, v13, s45, 0
	s_lshl_b32 s29, s46, 3
	v_and_b32_e32 v14, 0x7fff, v14
	s_andn2_b64 vcc, exec, s[4:5]
	v_or_b32_e32 v16, s6, v14
	s_cbranch_vccnz .Lrec_slowst
	buffer_store_short v16, v18, s[20:23], 0 offen
	s_branch .Lrec_stored
